# combo18 with phase 10 output stores interleaved into the combine (each 1 KB chunk stored as soon as it is computed)
# baseline (speedup 1.0000x reference)
.LBB0_1219:
	s_cmp_lt_i32 s48, 11
	s_cselect_b64 s[6:7], -1, 0
	s_and_b64 s[4:5], s[6:7], s[4:5]
	s_andn2_b64 vcc, exec, s[4:5]
	s_cbranch_vccnz .LBB0_1225
	s_load_dwordx4 s[4:7], s[0:1], 0xa8
	v_and_b32_e32 v1, 63, v0
	v_lshrrev_b32_e32 v5, 6, v0
	s_lshl_b32 s13, s2, 3
	v_readfirstlane_b32 s12, v5
	v_lshlrev_b32_e32 v2, 2, v1
	v_lshlrev_b32_e32 v3, 3, v1
	v_lshlrev_b32_e32 v4, 4, v1
	s_add_i32 s12, s12, s13
	v_lshl_add_u32 v5, v1, 11, s12
	v_lshlrev_b32_e32 v5, 3, v5
	v_cmp_gt_u32_e32 vcc, 8, v1
	s_waitcnt lgkmcnt(0)
	s_add_u32 s8, s6, 0x33c0a000
	s_addc_u32 s9, s7, 0
	s_add_u32 s10, s6, 0x33c2a000
	s_addc_u32 s11, s7, 0
	s_add_u32 s48, s6, 0x4744a000
	s_addc_u32 s49, s7, 0
	s_add_u32 s60, s6, 0x2b80a000
	s_addc_u32 s61, s7, 0
	s_lshl_b32 s14, s12, 12
	s_add_u32 s62, s60, s14
	s_addc_u32 s63, s61, 0
	s_lshl_b32 s14, s12, 13
	s_add_u32 s64, s4, s14
	s_addc_u32 s65, s5, 0
	s_and_saveexec_b64 s[14:15], vcc
	global_load_dwordx2 v[6:7], v5, s[8:9]
	global_load_dwordx2 v[8:9], v5, s[10:11]
	s_waitcnt vmcnt(1)
	v_ashrrev_i32_e32 v10, 16, v6
	v_ashrrev_i32_e32 v11, 16, v7
	v_lshlrev_b32_e32 v10, 2, v10
	v_lshlrev_b32_e32 v11, 2, v11
	v_add_u32_e32 v10, 0x24140, v10
	v_add_u32_e32 v11, 0x24140, v11
	ds_read_b32 v10, v10
	ds_read_b32 v11, v11
	v_and_b32_e32 v6, 0xffff, v6
	v_and_b32_e32 v7, 0xffff, v7
	s_waitcnt lgkmcnt(0)
	v_lshl_add_u32 v6, v10, 8, v6
	v_lshl_add_u32 v7, v11, 8, v7
	s_waitcnt vmcnt(0)
	s_mov_b64 exec, s[14:15]
	s_nop 1
	v_readlane_b32 s16, v6, 0
	v_readlane_b32 s24, v7, 0
	v_readlane_b32 s32, v8, 0
	v_readlane_b32 s40, v9, 0
	v_readlane_b32 s17, v6, 1
	v_readlane_b32 s25, v7, 1
	v_readlane_b32 s33, v8, 1
	v_readlane_b32 s41, v9, 1
	v_readlane_b32 s18, v6, 2
	v_readlane_b32 s26, v7, 2
	v_readlane_b32 s34, v8, 2
	v_readlane_b32 s42, v9, 2
	v_readlane_b32 s19, v6, 3
	v_readlane_b32 s27, v7, 3
	v_readlane_b32 s35, v8, 3
	v_readlane_b32 s43, v9, 3
	v_readlane_b32 s20, v6, 4
	v_readlane_b32 s28, v7, 4
	v_readlane_b32 s36, v8, 4
	v_readlane_b32 s44, v9, 4
	v_readlane_b32 s21, v6, 5
	v_readlane_b32 s29, v7, 5
	v_readlane_b32 s37, v8, 5
	v_readlane_b32 s45, v9, 5
	v_readlane_b32 s22, v6, 6
	v_readlane_b32 s30, v7, 6
	v_readlane_b32 s38, v8, 6
	v_readlane_b32 s46, v9, 6
	v_readlane_b32 s23, v6, 7
	v_readlane_b32 s31, v7, 7
	v_readlane_b32 s39, v8, 7
	v_readlane_b32 s47, v9, 7
	s_nop 3
	s_lshl_b32 s50, s16, 11
	s_add_u32 s50, s48, s50
	s_addc_u32 s51, s49, 0
	s_lshl_b32 s52, s24, 11
	s_add_u32 s52, s48, s52
	s_addc_u32 s53, s49, 0
	s_mov_b64 s[54:55], s[62:63]
	global_load_dword v64, v2, s[50:51]
	global_load_dword v65, v2, s[50:51] offset:256
	global_load_dword v66, v2, s[50:51] offset:512
	global_load_dword v67, v2, s[50:51] offset:768
	global_load_dword v68, v2, s[50:51] offset:1024
	global_load_dword v69, v2, s[50:51] offset:1280
	global_load_dword v70, v2, s[50:51] offset:1536
	global_load_dword v71, v2, s[50:51] offset:1792
	global_load_dword v72, v2, s[52:53]
	global_load_dword v73, v2, s[52:53] offset:256
	global_load_dword v74, v2, s[52:53] offset:512
	global_load_dword v75, v2, s[52:53] offset:768
	global_load_dword v76, v2, s[52:53] offset:1024
	global_load_dword v77, v2, s[52:53] offset:1280
	global_load_dword v78, v2, s[52:53] offset:1536
	global_load_dword v79, v2, s[52:53] offset:1792
	global_load_dwordx2 v[80:81], v3, s[54:55]
	global_load_dwordx2 v[82:83], v3, s[54:55] offset:512
	global_load_dwordx2 v[84:85], v3, s[54:55] offset:1024
	global_load_dwordx2 v[86:87], v3, s[54:55] offset:1536
	global_load_dwordx2 v[88:89], v3, s[54:55] offset:2048
	global_load_dwordx2 v[90:91], v3, s[54:55] offset:2560
	global_load_dwordx2 v[92:93], v3, s[54:55] offset:3072
	global_load_dwordx2 v[94:95], v3, s[54:55] offset:3584
	s_lshl_b32 s50, s17, 11
	s_add_u32 s50, s48, s50
	s_addc_u32 s51, s49, 0
	s_lshl_b32 s52, s25, 11
	s_add_u32 s52, s48, s52
	s_addc_u32 s53, s49, 0
	s_add_u32 s54, s62, 0x800000
	s_addc_u32 s55, s63, 0
	global_load_dword v96, v2, s[50:51]
	global_load_dword v97, v2, s[50:51] offset:256
	global_load_dword v98, v2, s[50:51] offset:512
	global_load_dword v99, v2, s[50:51] offset:768
	global_load_dword v100, v2, s[50:51] offset:1024
	global_load_dword v101, v2, s[50:51] offset:1280
	global_load_dword v102, v2, s[50:51] offset:1536
	global_load_dword v103, v2, s[50:51] offset:1792
	global_load_dword v104, v2, s[52:53]
	global_load_dword v105, v2, s[52:53] offset:256
	global_load_dword v106, v2, s[52:53] offset:512
	global_load_dword v107, v2, s[52:53] offset:768
	global_load_dword v108, v2, s[52:53] offset:1024
	global_load_dword v109, v2, s[52:53] offset:1280
	global_load_dword v110, v2, s[52:53] offset:1536
	global_load_dword v111, v2, s[52:53] offset:1792
	global_load_dwordx2 v[112:113], v3, s[54:55]
	global_load_dwordx2 v[114:115], v3, s[54:55] offset:512
	global_load_dwordx2 v[116:117], v3, s[54:55] offset:1024
	global_load_dwordx2 v[118:119], v3, s[54:55] offset:1536
	global_load_dwordx2 v[120:121], v3, s[54:55] offset:2048
	global_load_dwordx2 v[122:123], v3, s[54:55] offset:2560
	global_load_dwordx2 v[124:125], v3, s[54:55] offset:3072
	global_load_dwordx2 v[126:127], v3, s[54:55] offset:3584
	s_waitcnt vmcnt(24)
	s_lshl_b32 s50, s18, 11
	s_add_u32 s50, s48, s50
	s_addc_u32 s51, s49, 0
	s_lshl_b32 s52, s26, 11
	s_add_u32 s52, s48, s52
	s_addc_u32 s53, s49, 0
	s_add_u32 s54, s62, 0x1000000
	s_addc_u32 s55, s63, 0
	global_load_dword v128, v2, s[50:51]
	global_load_dword v129, v2, s[50:51] offset:256
	global_load_dword v130, v2, s[50:51] offset:512
	global_load_dword v131, v2, s[50:51] offset:768
	global_load_dword v132, v2, s[50:51] offset:1024
	global_load_dword v133, v2, s[50:51] offset:1280
	global_load_dword v134, v2, s[50:51] offset:1536
	global_load_dword v135, v2, s[50:51] offset:1792
	global_load_dword v136, v2, s[52:53]
	global_load_dword v137, v2, s[52:53] offset:256
	global_load_dword v138, v2, s[52:53] offset:512
	global_load_dword v139, v2, s[52:53] offset:768
	global_load_dword v140, v2, s[52:53] offset:1024
	global_load_dword v141, v2, s[52:53] offset:1280
	global_load_dword v142, v2, s[52:53] offset:1536
	global_load_dword v143, v2, s[52:53] offset:1792
	global_load_dwordx2 v[144:145], v3, s[54:55]
	global_load_dwordx2 v[146:147], v3, s[54:55] offset:512
	global_load_dwordx2 v[148:149], v3, s[54:55] offset:1024
	global_load_dwordx2 v[150:151], v3, s[54:55] offset:1536
	global_load_dwordx2 v[152:153], v3, s[54:55] offset:2048
	global_load_dwordx2 v[154:155], v3, s[54:55] offset:2560
	global_load_dwordx2 v[156:157], v3, s[54:55] offset:3072
	global_load_dwordx2 v[158:159], v3, s[54:55] offset:3584
	s_mov_b64 s[56:57], s[64:65]
	s_add_u32 s58, s56, 0x1000
	s_addc_u32 s59, s57, 0
	v_mov_b32_e32 v240, s32
	v_mov_b32_e32 v242, s40
	v_cvt_pk_f32_fp8_e32 v[224:225], v64
	v_cvt_pk_f32_fp8_sdwa v[226:227], v64 src0_sel:WORD_1
	v_cvt_pk_f32_fp8_e32 v[228:229], v72
	v_cvt_pk_f32_fp8_sdwa v[230:231], v72 src0_sel:WORD_1
	v_lshlrev_b32_e32 v192, 16, v80
	v_and_b32_e32 v193, 0xffff0000, v80
	v_lshlrev_b32_e32 v194, 16, v81
	v_and_b32_e32 v195, 0xffff0000, v81
	v_pk_fma_f32 v[192:193], v[224:225], v[240:241], v[192:193] op_sel_hi:[1,0,1]
	v_pk_fma_f32 v[194:195], v[226:227], v[240:241], v[194:195] op_sel_hi:[1,0,1]
	v_pk_fma_f32 v[192:193], v[228:229], v[242:243], v[192:193] op_sel_hi:[1,0,1]
	v_pk_fma_f32 v[194:195], v[230:231], v[242:243], v[194:195] op_sel_hi:[1,0,1]
	s_waitcnt vmcnt(55)
	global_store_dwordx4 v4, v[192:195], s[56:57]
	v_cvt_pk_f32_fp8_e32 v[232:233], v65
	v_cvt_pk_f32_fp8_sdwa v[234:235], v65 src0_sel:WORD_1
	v_cvt_pk_f32_fp8_e32 v[236:237], v73
	v_cvt_pk_f32_fp8_sdwa v[238:239], v73 src0_sel:WORD_1
	v_lshlrev_b32_e32 v196, 16, v82
	v_and_b32_e32 v197, 0xffff0000, v82
	v_lshlrev_b32_e32 v198, 16, v83
	v_and_b32_e32 v199, 0xffff0000, v83
	v_pk_fma_f32 v[196:197], v[232:233], v[240:241], v[196:197] op_sel_hi:[1,0,1]
	v_pk_fma_f32 v[198:199], v[234:235], v[240:241], v[198:199] op_sel_hi:[1,0,1]
	v_pk_fma_f32 v[196:197], v[236:237], v[242:243], v[196:197] op_sel_hi:[1,0,1]
	v_pk_fma_f32 v[198:199], v[238:239], v[242:243], v[198:199] op_sel_hi:[1,0,1]
	global_store_dwordx4 v4, v[196:199], s[56:57] offset:1024
	v_cvt_pk_f32_fp8_e32 v[224:225], v66
	v_cvt_pk_f32_fp8_sdwa v[226:227], v66 src0_sel:WORD_1
	v_cvt_pk_f32_fp8_e32 v[228:229], v74
	v_cvt_pk_f32_fp8_sdwa v[230:231], v74 src0_sel:WORD_1
	v_lshlrev_b32_e32 v200, 16, v84
	v_and_b32_e32 v201, 0xffff0000, v84
	v_lshlrev_b32_e32 v202, 16, v85
	v_and_b32_e32 v203, 0xffff0000, v85
	v_pk_fma_f32 v[200:201], v[224:225], v[240:241], v[200:201] op_sel_hi:[1,0,1]
	v_pk_fma_f32 v[202:203], v[226:227], v[240:241], v[202:203] op_sel_hi:[1,0,1]
	v_pk_fma_f32 v[200:201], v[228:229], v[242:243], v[200:201] op_sel_hi:[1,0,1]
	v_pk_fma_f32 v[202:203], v[230:231], v[242:243], v[202:203] op_sel_hi:[1,0,1]
	global_store_dwordx4 v4, v[200:203], s[56:57] offset:2048
	v_cvt_pk_f32_fp8_e32 v[232:233], v67
	v_cvt_pk_f32_fp8_sdwa v[234:235], v67 src0_sel:WORD_1
	v_cvt_pk_f32_fp8_e32 v[236:237], v75
	v_cvt_pk_f32_fp8_sdwa v[238:239], v75 src0_sel:WORD_1
	v_lshlrev_b32_e32 v204, 16, v86
	v_and_b32_e32 v205, 0xffff0000, v86
	v_lshlrev_b32_e32 v206, 16, v87
	v_and_b32_e32 v207, 0xffff0000, v87
	v_pk_fma_f32 v[204:205], v[232:233], v[240:241], v[204:205] op_sel_hi:[1,0,1]
	v_pk_fma_f32 v[206:207], v[234:235], v[240:241], v[206:207] op_sel_hi:[1,0,1]
	v_pk_fma_f32 v[204:205], v[236:237], v[242:243], v[204:205] op_sel_hi:[1,0,1]
	v_pk_fma_f32 v[206:207], v[238:239], v[242:243], v[206:207] op_sel_hi:[1,0,1]
	global_store_dwordx4 v4, v[204:207], s[56:57] offset:3072
	v_cvt_pk_f32_fp8_e32 v[224:225], v68
	v_cvt_pk_f32_fp8_sdwa v[226:227], v68 src0_sel:WORD_1
	v_cvt_pk_f32_fp8_e32 v[228:229], v76
	v_cvt_pk_f32_fp8_sdwa v[230:231], v76 src0_sel:WORD_1
	v_lshlrev_b32_e32 v208, 16, v88
	v_and_b32_e32 v209, 0xffff0000, v88
	v_lshlrev_b32_e32 v210, 16, v89
	v_and_b32_e32 v211, 0xffff0000, v89
	v_pk_fma_f32 v[208:209], v[224:225], v[240:241], v[208:209] op_sel_hi:[1,0,1]
	v_pk_fma_f32 v[210:211], v[226:227], v[240:241], v[210:211] op_sel_hi:[1,0,1]
	v_pk_fma_f32 v[208:209], v[228:229], v[242:243], v[208:209] op_sel_hi:[1,0,1]
	v_pk_fma_f32 v[210:211], v[230:231], v[242:243], v[210:211] op_sel_hi:[1,0,1]
	global_store_dwordx4 v4, v[208:211], s[58:59]
	v_cvt_pk_f32_fp8_e32 v[232:233], v69
	v_cvt_pk_f32_fp8_sdwa v[234:235], v69 src0_sel:WORD_1
	v_cvt_pk_f32_fp8_e32 v[236:237], v77
	v_cvt_pk_f32_fp8_sdwa v[238:239], v77 src0_sel:WORD_1
	v_lshlrev_b32_e32 v212, 16, v90
	v_and_b32_e32 v213, 0xffff0000, v90
	v_lshlrev_b32_e32 v214, 16, v91
	v_and_b32_e32 v215, 0xffff0000, v91
	v_pk_fma_f32 v[212:213], v[232:233], v[240:241], v[212:213] op_sel_hi:[1,0,1]
	v_pk_fma_f32 v[214:215], v[234:235], v[240:241], v[214:215] op_sel_hi:[1,0,1]
	v_pk_fma_f32 v[212:213], v[236:237], v[242:243], v[212:213] op_sel_hi:[1,0,1]
	v_pk_fma_f32 v[214:215], v[238:239], v[242:243], v[214:215] op_sel_hi:[1,0,1]
	global_store_dwordx4 v4, v[212:215], s[58:59] offset:1024
	v_cvt_pk_f32_fp8_e32 v[224:225], v70
	v_cvt_pk_f32_fp8_sdwa v[226:227], v70 src0_sel:WORD_1
	v_cvt_pk_f32_fp8_e32 v[228:229], v78
	v_cvt_pk_f32_fp8_sdwa v[230:231], v78 src0_sel:WORD_1
	v_lshlrev_b32_e32 v216, 16, v92
	v_and_b32_e32 v217, 0xffff0000, v92
	v_lshlrev_b32_e32 v218, 16, v93
	v_and_b32_e32 v219, 0xffff0000, v93
	v_pk_fma_f32 v[216:217], v[224:225], v[240:241], v[216:217] op_sel_hi:[1,0,1]
	v_pk_fma_f32 v[218:219], v[226:227], v[240:241], v[218:219] op_sel_hi:[1,0,1]
	v_pk_fma_f32 v[216:217], v[228:229], v[242:243], v[216:217] op_sel_hi:[1,0,1]
	v_pk_fma_f32 v[218:219], v[230:231], v[242:243], v[218:219] op_sel_hi:[1,0,1]
	global_store_dwordx4 v4, v[216:219], s[58:59] offset:2048
	v_cvt_pk_f32_fp8_e32 v[232:233], v71
	v_cvt_pk_f32_fp8_sdwa v[234:235], v71 src0_sel:WORD_1
	v_cvt_pk_f32_fp8_e32 v[236:237], v79
	v_cvt_pk_f32_fp8_sdwa v[238:239], v79 src0_sel:WORD_1
	v_lshlrev_b32_e32 v220, 16, v94
	v_and_b32_e32 v221, 0xffff0000, v94
	v_lshlrev_b32_e32 v222, 16, v95
	v_and_b32_e32 v223, 0xffff0000, v95
	v_pk_fma_f32 v[220:221], v[232:233], v[240:241], v[220:221] op_sel_hi:[1,0,1]
	v_pk_fma_f32 v[222:223], v[234:235], v[240:241], v[222:223] op_sel_hi:[1,0,1]
	v_pk_fma_f32 v[220:221], v[236:237], v[242:243], v[220:221] op_sel_hi:[1,0,1]
	v_pk_fma_f32 v[222:223], v[238:239], v[242:243], v[222:223] op_sel_hi:[1,0,1]
	global_store_dwordx4 v4, v[220:223], s[58:59] offset:3072
	s_waitcnt vmcnt(32)
	s_lshl_b32 s50, s19, 11
	s_add_u32 s50, s48, s50
	s_addc_u32 s51, s49, 0
	s_lshl_b32 s52, s27, 11
	s_add_u32 s52, s48, s52
	s_addc_u32 s53, s49, 0
	s_add_u32 s54, s62, 0x1800000
	s_addc_u32 s55, s63, 0
	global_load_dword v64, v2, s[50:51]
	global_load_dword v65, v2, s[50:51] offset:256
	global_load_dword v66, v2, s[50:51] offset:512
	global_load_dword v67, v2, s[50:51] offset:768
	global_load_dword v68, v2, s[50:51] offset:1024
	global_load_dword v69, v2, s[50:51] offset:1280
	global_load_dword v70, v2, s[50:51] offset:1536
	global_load_dword v71, v2, s[50:51] offset:1792
	global_load_dword v72, v2, s[52:53]
	global_load_dword v73, v2, s[52:53] offset:256
	global_load_dword v74, v2, s[52:53] offset:512
	global_load_dword v75, v2, s[52:53] offset:768
	global_load_dword v76, v2, s[52:53] offset:1024
	global_load_dword v77, v2, s[52:53] offset:1280
	global_load_dword v78, v2, s[52:53] offset:1536
	global_load_dword v79, v2, s[52:53] offset:1792
	global_load_dwordx2 v[80:81], v3, s[54:55]
	global_load_dwordx2 v[82:83], v3, s[54:55] offset:512
	global_load_dwordx2 v[84:85], v3, s[54:55] offset:1024
	global_load_dwordx2 v[86:87], v3, s[54:55] offset:1536
	global_load_dwordx2 v[88:89], v3, s[54:55] offset:2048
	global_load_dwordx2 v[90:91], v3, s[54:55] offset:2560
	global_load_dwordx2 v[92:93], v3, s[54:55] offset:3072
	global_load_dwordx2 v[94:95], v3, s[54:55] offset:3584
	s_add_u32 s56, s64, 0x1000000
	s_addc_u32 s57, s65, 0
	s_add_u32 s58, s56, 0x1000
	s_addc_u32 s59, s57, 0
	v_mov_b32_e32 v240, s33
	v_mov_b32_e32 v242, s41
	v_cvt_pk_f32_fp8_e32 v[224:225], v96
	v_cvt_pk_f32_fp8_sdwa v[226:227], v96 src0_sel:WORD_1
	v_cvt_pk_f32_fp8_e32 v[228:229], v104
	v_cvt_pk_f32_fp8_sdwa v[230:231], v104 src0_sel:WORD_1
	v_lshlrev_b32_e32 v192, 16, v112
	v_and_b32_e32 v193, 0xffff0000, v112
	v_lshlrev_b32_e32 v194, 16, v113
	v_and_b32_e32 v195, 0xffff0000, v113
	v_pk_fma_f32 v[192:193], v[224:225], v[240:241], v[192:193] op_sel_hi:[1,0,1]
	v_pk_fma_f32 v[194:195], v[226:227], v[240:241], v[194:195] op_sel_hi:[1,0,1]
	v_pk_fma_f32 v[192:193], v[228:229], v[242:243], v[192:193] op_sel_hi:[1,0,1]
	v_pk_fma_f32 v[194:195], v[230:231], v[242:243], v[194:195] op_sel_hi:[1,0,1]
	s_waitcnt vmcnt(55)
	global_store_dwordx4 v4, v[192:195], s[56:57]
	v_cvt_pk_f32_fp8_e32 v[232:233], v97
	v_cvt_pk_f32_fp8_sdwa v[234:235], v97 src0_sel:WORD_1
	v_cvt_pk_f32_fp8_e32 v[236:237], v105
	v_cvt_pk_f32_fp8_sdwa v[238:239], v105 src0_sel:WORD_1
	v_lshlrev_b32_e32 v196, 16, v114
	v_and_b32_e32 v197, 0xffff0000, v114
	v_lshlrev_b32_e32 v198, 16, v115
	v_and_b32_e32 v199, 0xffff0000, v115
	v_pk_fma_f32 v[196:197], v[232:233], v[240:241], v[196:197] op_sel_hi:[1,0,1]
	v_pk_fma_f32 v[198:199], v[234:235], v[240:241], v[198:199] op_sel_hi:[1,0,1]
	v_pk_fma_f32 v[196:197], v[236:237], v[242:243], v[196:197] op_sel_hi:[1,0,1]
	v_pk_fma_f32 v[198:199], v[238:239], v[242:243], v[198:199] op_sel_hi:[1,0,1]
	global_store_dwordx4 v4, v[196:199], s[56:57] offset:1024
	v_cvt_pk_f32_fp8_e32 v[224:225], v98
	v_cvt_pk_f32_fp8_sdwa v[226:227], v98 src0_sel:WORD_1
	v_cvt_pk_f32_fp8_e32 v[228:229], v106
	v_cvt_pk_f32_fp8_sdwa v[230:231], v106 src0_sel:WORD_1
	v_lshlrev_b32_e32 v200, 16, v116
	v_and_b32_e32 v201, 0xffff0000, v116
	v_lshlrev_b32_e32 v202, 16, v117
	v_and_b32_e32 v203, 0xffff0000, v117
	v_pk_fma_f32 v[200:201], v[224:225], v[240:241], v[200:201] op_sel_hi:[1,0,1]
	v_pk_fma_f32 v[202:203], v[226:227], v[240:241], v[202:203] op_sel_hi:[1,0,1]
	v_pk_fma_f32 v[200:201], v[228:229], v[242:243], v[200:201] op_sel_hi:[1,0,1]
	v_pk_fma_f32 v[202:203], v[230:231], v[242:243], v[202:203] op_sel_hi:[1,0,1]
	global_store_dwordx4 v4, v[200:203], s[56:57] offset:2048
	v_cvt_pk_f32_fp8_e32 v[232:233], v99
	v_cvt_pk_f32_fp8_sdwa v[234:235], v99 src0_sel:WORD_1
	v_cvt_pk_f32_fp8_e32 v[236:237], v107
	v_cvt_pk_f32_fp8_sdwa v[238:239], v107 src0_sel:WORD_1
	v_lshlrev_b32_e32 v204, 16, v118
	v_and_b32_e32 v205, 0xffff0000, v118
	v_lshlrev_b32_e32 v206, 16, v119
	v_and_b32_e32 v207, 0xffff0000, v119
	v_pk_fma_f32 v[204:205], v[232:233], v[240:241], v[204:205] op_sel_hi:[1,0,1]
	v_pk_fma_f32 v[206:207], v[234:235], v[240:241], v[206:207] op_sel_hi:[1,0,1]
	v_pk_fma_f32 v[204:205], v[236:237], v[242:243], v[204:205] op_sel_hi:[1,0,1]
	v_pk_fma_f32 v[206:207], v[238:239], v[242:243], v[206:207] op_sel_hi:[1,0,1]
	global_store_dwordx4 v4, v[204:207], s[56:57] offset:3072
	v_cvt_pk_f32_fp8_e32 v[224:225], v100
	v_cvt_pk_f32_fp8_sdwa v[226:227], v100 src0_sel:WORD_1
	v_cvt_pk_f32_fp8_e32 v[228:229], v108
	v_cvt_pk_f32_fp8_sdwa v[230:231], v108 src0_sel:WORD_1
	v_lshlrev_b32_e32 v208, 16, v120
	v_and_b32_e32 v209, 0xffff0000, v120
	v_lshlrev_b32_e32 v210, 16, v121
	v_and_b32_e32 v211, 0xffff0000, v121
	v_pk_fma_f32 v[208:209], v[224:225], v[240:241], v[208:209] op_sel_hi:[1,0,1]
	v_pk_fma_f32 v[210:211], v[226:227], v[240:241], v[210:211] op_sel_hi:[1,0,1]
	v_pk_fma_f32 v[208:209], v[228:229], v[242:243], v[208:209] op_sel_hi:[1,0,1]
	v_pk_fma_f32 v[210:211], v[230:231], v[242:243], v[210:211] op_sel_hi:[1,0,1]
	global_store_dwordx4 v4, v[208:211], s[58:59]
	v_cvt_pk_f32_fp8_e32 v[232:233], v101
	v_cvt_pk_f32_fp8_sdwa v[234:235], v101 src0_sel:WORD_1
	v_cvt_pk_f32_fp8_e32 v[236:237], v109
	v_cvt_pk_f32_fp8_sdwa v[238:239], v109 src0_sel:WORD_1
	v_lshlrev_b32_e32 v212, 16, v122
	v_and_b32_e32 v213, 0xffff0000, v122
	v_lshlrev_b32_e32 v214, 16, v123
	v_and_b32_e32 v215, 0xffff0000, v123
	v_pk_fma_f32 v[212:213], v[232:233], v[240:241], v[212:213] op_sel_hi:[1,0,1]
	v_pk_fma_f32 v[214:215], v[234:235], v[240:241], v[214:215] op_sel_hi:[1,0,1]
	v_pk_fma_f32 v[212:213], v[236:237], v[242:243], v[212:213] op_sel_hi:[1,0,1]
	v_pk_fma_f32 v[214:215], v[238:239], v[242:243], v[214:215] op_sel_hi:[1,0,1]
	global_store_dwordx4 v4, v[212:215], s[58:59] offset:1024
	v_cvt_pk_f32_fp8_e32 v[224:225], v102
	v_cvt_pk_f32_fp8_sdwa v[226:227], v102 src0_sel:WORD_1
	v_cvt_pk_f32_fp8_e32 v[228:229], v110
	v_cvt_pk_f32_fp8_sdwa v[230:231], v110 src0_sel:WORD_1
	v_lshlrev_b32_e32 v216, 16, v124
	v_and_b32_e32 v217, 0xffff0000, v124
	v_lshlrev_b32_e32 v218, 16, v125
	v_and_b32_e32 v219, 0xffff0000, v125
	v_pk_fma_f32 v[216:217], v[224:225], v[240:241], v[216:217] op_sel_hi:[1,0,1]
	v_pk_fma_f32 v[218:219], v[226:227], v[240:241], v[218:219] op_sel_hi:[1,0,1]
	v_pk_fma_f32 v[216:217], v[228:229], v[242:243], v[216:217] op_sel_hi:[1,0,1]
	v_pk_fma_f32 v[218:219], v[230:231], v[242:243], v[218:219] op_sel_hi:[1,0,1]
	global_store_dwordx4 v4, v[216:219], s[58:59] offset:2048
	v_cvt_pk_f32_fp8_e32 v[232:233], v103
	v_cvt_pk_f32_fp8_sdwa v[234:235], v103 src0_sel:WORD_1
	v_cvt_pk_f32_fp8_e32 v[236:237], v111
	v_cvt_pk_f32_fp8_sdwa v[238:239], v111 src0_sel:WORD_1
	v_lshlrev_b32_e32 v220, 16, v126
	v_and_b32_e32 v221, 0xffff0000, v126
	v_lshlrev_b32_e32 v222, 16, v127
	v_and_b32_e32 v223, 0xffff0000, v127
	v_pk_fma_f32 v[220:221], v[232:233], v[240:241], v[220:221] op_sel_hi:[1,0,1]
	v_pk_fma_f32 v[222:223], v[234:235], v[240:241], v[222:223] op_sel_hi:[1,0,1]
	v_pk_fma_f32 v[220:221], v[236:237], v[242:243], v[220:221] op_sel_hi:[1,0,1]
	v_pk_fma_f32 v[222:223], v[238:239], v[242:243], v[222:223] op_sel_hi:[1,0,1]
	global_store_dwordx4 v4, v[220:223], s[58:59] offset:3072
	s_waitcnt vmcnt(32)
	s_lshl_b32 s50, s20, 11
	s_add_u32 s50, s48, s50
	s_addc_u32 s51, s49, 0
	s_lshl_b32 s52, s28, 11
	s_add_u32 s52, s48, s52
	s_addc_u32 s53, s49, 0
	s_add_u32 s54, s62, 0x2000000
	s_addc_u32 s55, s63, 0
	global_load_dword v96, v2, s[50:51]
	global_load_dword v97, v2, s[50:51] offset:256
	global_load_dword v98, v2, s[50:51] offset:512
	global_load_dword v99, v2, s[50:51] offset:768
	global_load_dword v100, v2, s[50:51] offset:1024
	global_load_dword v101, v2, s[50:51] offset:1280
	global_load_dword v102, v2, s[50:51] offset:1536
	global_load_dword v103, v2, s[50:51] offset:1792
	global_load_dword v104, v2, s[52:53]
	global_load_dword v105, v2, s[52:53] offset:256
	global_load_dword v106, v2, s[52:53] offset:512
	global_load_dword v107, v2, s[52:53] offset:768
	global_load_dword v108, v2, s[52:53] offset:1024
	global_load_dword v109, v2, s[52:53] offset:1280
	global_load_dword v110, v2, s[52:53] offset:1536
	global_load_dword v111, v2, s[52:53] offset:1792
	global_load_dwordx2 v[112:113], v3, s[54:55]
	global_load_dwordx2 v[114:115], v3, s[54:55] offset:512
	global_load_dwordx2 v[116:117], v3, s[54:55] offset:1024
	global_load_dwordx2 v[118:119], v3, s[54:55] offset:1536
	global_load_dwordx2 v[120:121], v3, s[54:55] offset:2048
	global_load_dwordx2 v[122:123], v3, s[54:55] offset:2560
	global_load_dwordx2 v[124:125], v3, s[54:55] offset:3072
	global_load_dwordx2 v[126:127], v3, s[54:55] offset:3584
	s_add_u32 s56, s64, 0x2000000
	s_addc_u32 s57, s65, 0
	s_add_u32 s58, s56, 0x1000
	s_addc_u32 s59, s57, 0
	v_mov_b32_e32 v240, s34
	v_mov_b32_e32 v242, s42
	v_cvt_pk_f32_fp8_e32 v[224:225], v128
	v_cvt_pk_f32_fp8_sdwa v[226:227], v128 src0_sel:WORD_1
	v_cvt_pk_f32_fp8_e32 v[228:229], v136
	v_cvt_pk_f32_fp8_sdwa v[230:231], v136 src0_sel:WORD_1
	v_lshlrev_b32_e32 v192, 16, v144
	v_and_b32_e32 v193, 0xffff0000, v144
	v_lshlrev_b32_e32 v194, 16, v145
	v_and_b32_e32 v195, 0xffff0000, v145
	v_pk_fma_f32 v[192:193], v[224:225], v[240:241], v[192:193] op_sel_hi:[1,0,1]
	v_pk_fma_f32 v[194:195], v[226:227], v[240:241], v[194:195] op_sel_hi:[1,0,1]
	v_pk_fma_f32 v[192:193], v[228:229], v[242:243], v[192:193] op_sel_hi:[1,0,1]
	v_pk_fma_f32 v[194:195], v[230:231], v[242:243], v[194:195] op_sel_hi:[1,0,1]
	s_waitcnt vmcnt(55)
	global_store_dwordx4 v4, v[192:195], s[56:57]
	v_cvt_pk_f32_fp8_e32 v[232:233], v129
	v_cvt_pk_f32_fp8_sdwa v[234:235], v129 src0_sel:WORD_1
	v_cvt_pk_f32_fp8_e32 v[236:237], v137
	v_cvt_pk_f32_fp8_sdwa v[238:239], v137 src0_sel:WORD_1
	v_lshlrev_b32_e32 v196, 16, v146
	v_and_b32_e32 v197, 0xffff0000, v146
	v_lshlrev_b32_e32 v198, 16, v147
	v_and_b32_e32 v199, 0xffff0000, v147
	v_pk_fma_f32 v[196:197], v[232:233], v[240:241], v[196:197] op_sel_hi:[1,0,1]
	v_pk_fma_f32 v[198:199], v[234:235], v[240:241], v[198:199] op_sel_hi:[1,0,1]
	v_pk_fma_f32 v[196:197], v[236:237], v[242:243], v[196:197] op_sel_hi:[1,0,1]
	v_pk_fma_f32 v[198:199], v[238:239], v[242:243], v[198:199] op_sel_hi:[1,0,1]
	global_store_dwordx4 v4, v[196:199], s[56:57] offset:1024
	v_cvt_pk_f32_fp8_e32 v[224:225], v130
	v_cvt_pk_f32_fp8_sdwa v[226:227], v130 src0_sel:WORD_1
	v_cvt_pk_f32_fp8_e32 v[228:229], v138
	v_cvt_pk_f32_fp8_sdwa v[230:231], v138 src0_sel:WORD_1
	v_lshlrev_b32_e32 v200, 16, v148
	v_and_b32_e32 v201, 0xffff0000, v148
	v_lshlrev_b32_e32 v202, 16, v149
	v_and_b32_e32 v203, 0xffff0000, v149
	v_pk_fma_f32 v[200:201], v[224:225], v[240:241], v[200:201] op_sel_hi:[1,0,1]
	v_pk_fma_f32 v[202:203], v[226:227], v[240:241], v[202:203] op_sel_hi:[1,0,1]
	v_pk_fma_f32 v[200:201], v[228:229], v[242:243], v[200:201] op_sel_hi:[1,0,1]
	v_pk_fma_f32 v[202:203], v[230:231], v[242:243], v[202:203] op_sel_hi:[1,0,1]
	global_store_dwordx4 v4, v[200:203], s[56:57] offset:2048
	v_cvt_pk_f32_fp8_e32 v[232:233], v131
	v_cvt_pk_f32_fp8_sdwa v[234:235], v131 src0_sel:WORD_1
	v_cvt_pk_f32_fp8_e32 v[236:237], v139
	v_cvt_pk_f32_fp8_sdwa v[238:239], v139 src0_sel:WORD_1
	v_lshlrev_b32_e32 v204, 16, v150
	v_and_b32_e32 v205, 0xffff0000, v150
	v_lshlrev_b32_e32 v206, 16, v151
	v_and_b32_e32 v207, 0xffff0000, v151
	v_pk_fma_f32 v[204:205], v[232:233], v[240:241], v[204:205] op_sel_hi:[1,0,1]
	v_pk_fma_f32 v[206:207], v[234:235], v[240:241], v[206:207] op_sel_hi:[1,0,1]
	v_pk_fma_f32 v[204:205], v[236:237], v[242:243], v[204:205] op_sel_hi:[1,0,1]
	v_pk_fma_f32 v[206:207], v[238:239], v[242:243], v[206:207] op_sel_hi:[1,0,1]
	global_store_dwordx4 v4, v[204:207], s[56:57] offset:3072
	v_cvt_pk_f32_fp8_e32 v[224:225], v132
	v_cvt_pk_f32_fp8_sdwa v[226:227], v132 src0_sel:WORD_1
	v_cvt_pk_f32_fp8_e32 v[228:229], v140
	v_cvt_pk_f32_fp8_sdwa v[230:231], v140 src0_sel:WORD_1
	v_lshlrev_b32_e32 v208, 16, v152
	v_and_b32_e32 v209, 0xffff0000, v152
	v_lshlrev_b32_e32 v210, 16, v153
	v_and_b32_e32 v211, 0xffff0000, v153
	v_pk_fma_f32 v[208:209], v[224:225], v[240:241], v[208:209] op_sel_hi:[1,0,1]
	v_pk_fma_f32 v[210:211], v[226:227], v[240:241], v[210:211] op_sel_hi:[1,0,1]
	v_pk_fma_f32 v[208:209], v[228:229], v[242:243], v[208:209] op_sel_hi:[1,0,1]
	v_pk_fma_f32 v[210:211], v[230:231], v[242:243], v[210:211] op_sel_hi:[1,0,1]
	global_store_dwordx4 v4, v[208:211], s[58:59]
	v_cvt_pk_f32_fp8_e32 v[232:233], v133
	v_cvt_pk_f32_fp8_sdwa v[234:235], v133 src0_sel:WORD_1
	v_cvt_pk_f32_fp8_e32 v[236:237], v141
	v_cvt_pk_f32_fp8_sdwa v[238:239], v141 src0_sel:WORD_1
	v_lshlrev_b32_e32 v212, 16, v154
	v_and_b32_e32 v213, 0xffff0000, v154
	v_lshlrev_b32_e32 v214, 16, v155
	v_and_b32_e32 v215, 0xffff0000, v155
	v_pk_fma_f32 v[212:213], v[232:233], v[240:241], v[212:213] op_sel_hi:[1,0,1]
	v_pk_fma_f32 v[214:215], v[234:235], v[240:241], v[214:215] op_sel_hi:[1,0,1]
	v_pk_fma_f32 v[212:213], v[236:237], v[242:243], v[212:213] op_sel_hi:[1,0,1]
	v_pk_fma_f32 v[214:215], v[238:239], v[242:243], v[214:215] op_sel_hi:[1,0,1]
	global_store_dwordx4 v4, v[212:215], s[58:59] offset:1024
	v_cvt_pk_f32_fp8_e32 v[224:225], v134
	v_cvt_pk_f32_fp8_sdwa v[226:227], v134 src0_sel:WORD_1
	v_cvt_pk_f32_fp8_e32 v[228:229], v142
	v_cvt_pk_f32_fp8_sdwa v[230:231], v142 src0_sel:WORD_1
	v_lshlrev_b32_e32 v216, 16, v156
	v_and_b32_e32 v217, 0xffff0000, v156
	v_lshlrev_b32_e32 v218, 16, v157
	v_and_b32_e32 v219, 0xffff0000, v157
	v_pk_fma_f32 v[216:217], v[224:225], v[240:241], v[216:217] op_sel_hi:[1,0,1]
	v_pk_fma_f32 v[218:219], v[226:227], v[240:241], v[218:219] op_sel_hi:[1,0,1]
	v_pk_fma_f32 v[216:217], v[228:229], v[242:243], v[216:217] op_sel_hi:[1,0,1]
	v_pk_fma_f32 v[218:219], v[230:231], v[242:243], v[218:219] op_sel_hi:[1,0,1]
	global_store_dwordx4 v4, v[216:219], s[58:59] offset:2048
	v_cvt_pk_f32_fp8_e32 v[232:233], v135
	v_cvt_pk_f32_fp8_sdwa v[234:235], v135 src0_sel:WORD_1
	v_cvt_pk_f32_fp8_e32 v[236:237], v143
	v_cvt_pk_f32_fp8_sdwa v[238:239], v143 src0_sel:WORD_1
	v_lshlrev_b32_e32 v220, 16, v158
	v_and_b32_e32 v221, 0xffff0000, v158
	v_lshlrev_b32_e32 v222, 16, v159
	v_and_b32_e32 v223, 0xffff0000, v159
	v_pk_fma_f32 v[220:221], v[232:233], v[240:241], v[220:221] op_sel_hi:[1,0,1]
	v_pk_fma_f32 v[222:223], v[234:235], v[240:241], v[222:223] op_sel_hi:[1,0,1]
	v_pk_fma_f32 v[220:221], v[236:237], v[242:243], v[220:221] op_sel_hi:[1,0,1]
	v_pk_fma_f32 v[222:223], v[238:239], v[242:243], v[222:223] op_sel_hi:[1,0,1]
	global_store_dwordx4 v4, v[220:223], s[58:59] offset:3072
	s_waitcnt vmcnt(32)
	s_lshl_b32 s50, s21, 11
	s_add_u32 s50, s48, s50
	s_addc_u32 s51, s49, 0
	s_lshl_b32 s52, s29, 11
	s_add_u32 s52, s48, s52
	s_addc_u32 s53, s49, 0
	s_add_u32 s54, s62, 0x2800000
	s_addc_u32 s55, s63, 0
	global_load_dword v128, v2, s[50:51]
	global_load_dword v129, v2, s[50:51] offset:256
	global_load_dword v130, v2, s[50:51] offset:512
	global_load_dword v131, v2, s[50:51] offset:768
	global_load_dword v132, v2, s[50:51] offset:1024
	global_load_dword v133, v2, s[50:51] offset:1280
	global_load_dword v134, v2, s[50:51] offset:1536
	global_load_dword v135, v2, s[50:51] offset:1792
	global_load_dword v136, v2, s[52:53]
	global_load_dword v137, v2, s[52:53] offset:256
	global_load_dword v138, v2, s[52:53] offset:512
	global_load_dword v139, v2, s[52:53] offset:768
	global_load_dword v140, v2, s[52:53] offset:1024
	global_load_dword v141, v2, s[52:53] offset:1280
	global_load_dword v142, v2, s[52:53] offset:1536
	global_load_dword v143, v2, s[52:53] offset:1792
	global_load_dwordx2 v[144:145], v3, s[54:55]
	global_load_dwordx2 v[146:147], v3, s[54:55] offset:512
	global_load_dwordx2 v[148:149], v3, s[54:55] offset:1024
	global_load_dwordx2 v[150:151], v3, s[54:55] offset:1536
	global_load_dwordx2 v[152:153], v3, s[54:55] offset:2048
	global_load_dwordx2 v[154:155], v3, s[54:55] offset:2560
	global_load_dwordx2 v[156:157], v3, s[54:55] offset:3072
	global_load_dwordx2 v[158:159], v3, s[54:55] offset:3584
	s_add_u32 s56, s64, 0x3000000
	s_addc_u32 s57, s65, 0
	s_add_u32 s58, s56, 0x1000
	s_addc_u32 s59, s57, 0
	v_mov_b32_e32 v240, s35
	v_mov_b32_e32 v242, s43
	v_cvt_pk_f32_fp8_e32 v[224:225], v64
	v_cvt_pk_f32_fp8_sdwa v[226:227], v64 src0_sel:WORD_1
	v_cvt_pk_f32_fp8_e32 v[228:229], v72
	v_cvt_pk_f32_fp8_sdwa v[230:231], v72 src0_sel:WORD_1
	v_lshlrev_b32_e32 v192, 16, v80
	v_and_b32_e32 v193, 0xffff0000, v80
	v_lshlrev_b32_e32 v194, 16, v81
	v_and_b32_e32 v195, 0xffff0000, v81
	v_pk_fma_f32 v[192:193], v[224:225], v[240:241], v[192:193] op_sel_hi:[1,0,1]
	v_pk_fma_f32 v[194:195], v[226:227], v[240:241], v[194:195] op_sel_hi:[1,0,1]
	v_pk_fma_f32 v[192:193], v[228:229], v[242:243], v[192:193] op_sel_hi:[1,0,1]
	v_pk_fma_f32 v[194:195], v[230:231], v[242:243], v[194:195] op_sel_hi:[1,0,1]
	s_waitcnt vmcnt(55)
	global_store_dwordx4 v4, v[192:195], s[56:57]
	v_cvt_pk_f32_fp8_e32 v[232:233], v65
	v_cvt_pk_f32_fp8_sdwa v[234:235], v65 src0_sel:WORD_1
	v_cvt_pk_f32_fp8_e32 v[236:237], v73
	v_cvt_pk_f32_fp8_sdwa v[238:239], v73 src0_sel:WORD_1
	v_lshlrev_b32_e32 v196, 16, v82
	v_and_b32_e32 v197, 0xffff0000, v82
	v_lshlrev_b32_e32 v198, 16, v83
	v_and_b32_e32 v199, 0xffff0000, v83
	v_pk_fma_f32 v[196:197], v[232:233], v[240:241], v[196:197] op_sel_hi:[1,0,1]
	v_pk_fma_f32 v[198:199], v[234:235], v[240:241], v[198:199] op_sel_hi:[1,0,1]
	v_pk_fma_f32 v[196:197], v[236:237], v[242:243], v[196:197] op_sel_hi:[1,0,1]
	v_pk_fma_f32 v[198:199], v[238:239], v[242:243], v[198:199] op_sel_hi:[1,0,1]
	global_store_dwordx4 v4, v[196:199], s[56:57] offset:1024
	v_cvt_pk_f32_fp8_e32 v[224:225], v66
	v_cvt_pk_f32_fp8_sdwa v[226:227], v66 src0_sel:WORD_1
	v_cvt_pk_f32_fp8_e32 v[228:229], v74
	v_cvt_pk_f32_fp8_sdwa v[230:231], v74 src0_sel:WORD_1
	v_lshlrev_b32_e32 v200, 16, v84
	v_and_b32_e32 v201, 0xffff0000, v84
	v_lshlrev_b32_e32 v202, 16, v85
	v_and_b32_e32 v203, 0xffff0000, v85
	v_pk_fma_f32 v[200:201], v[224:225], v[240:241], v[200:201] op_sel_hi:[1,0,1]
	v_pk_fma_f32 v[202:203], v[226:227], v[240:241], v[202:203] op_sel_hi:[1,0,1]
	v_pk_fma_f32 v[200:201], v[228:229], v[242:243], v[200:201] op_sel_hi:[1,0,1]
	v_pk_fma_f32 v[202:203], v[230:231], v[242:243], v[202:203] op_sel_hi:[1,0,1]
	global_store_dwordx4 v4, v[200:203], s[56:57] offset:2048
	v_cvt_pk_f32_fp8_e32 v[232:233], v67
	v_cvt_pk_f32_fp8_sdwa v[234:235], v67 src0_sel:WORD_1
	v_cvt_pk_f32_fp8_e32 v[236:237], v75
	v_cvt_pk_f32_fp8_sdwa v[238:239], v75 src0_sel:WORD_1
	v_lshlrev_b32_e32 v204, 16, v86
	v_and_b32_e32 v205, 0xffff0000, v86
	v_lshlrev_b32_e32 v206, 16, v87
	v_and_b32_e32 v207, 0xffff0000, v87
	v_pk_fma_f32 v[204:205], v[232:233], v[240:241], v[204:205] op_sel_hi:[1,0,1]
	v_pk_fma_f32 v[206:207], v[234:235], v[240:241], v[206:207] op_sel_hi:[1,0,1]
	v_pk_fma_f32 v[204:205], v[236:237], v[242:243], v[204:205] op_sel_hi:[1,0,1]
	v_pk_fma_f32 v[206:207], v[238:239], v[242:243], v[206:207] op_sel_hi:[1,0,1]
	global_store_dwordx4 v4, v[204:207], s[56:57] offset:3072
	v_cvt_pk_f32_fp8_e32 v[224:225], v68
	v_cvt_pk_f32_fp8_sdwa v[226:227], v68 src0_sel:WORD_1
	v_cvt_pk_f32_fp8_e32 v[228:229], v76
	v_cvt_pk_f32_fp8_sdwa v[230:231], v76 src0_sel:WORD_1
	v_lshlrev_b32_e32 v208, 16, v88
	v_and_b32_e32 v209, 0xffff0000, v88
	v_lshlrev_b32_e32 v210, 16, v89
	v_and_b32_e32 v211, 0xffff0000, v89
	v_pk_fma_f32 v[208:209], v[224:225], v[240:241], v[208:209] op_sel_hi:[1,0,1]
	v_pk_fma_f32 v[210:211], v[226:227], v[240:241], v[210:211] op_sel_hi:[1,0,1]
	v_pk_fma_f32 v[208:209], v[228:229], v[242:243], v[208:209] op_sel_hi:[1,0,1]
	v_pk_fma_f32 v[210:211], v[230:231], v[242:243], v[210:211] op_sel_hi:[1,0,1]
	global_store_dwordx4 v4, v[208:211], s[58:59]
	v_cvt_pk_f32_fp8_e32 v[232:233], v69
	v_cvt_pk_f32_fp8_sdwa v[234:235], v69 src0_sel:WORD_1
	v_cvt_pk_f32_fp8_e32 v[236:237], v77
	v_cvt_pk_f32_fp8_sdwa v[238:239], v77 src0_sel:WORD_1
	v_lshlrev_b32_e32 v212, 16, v90
	v_and_b32_e32 v213, 0xffff0000, v90
	v_lshlrev_b32_e32 v214, 16, v91
	v_and_b32_e32 v215, 0xffff0000, v91
	v_pk_fma_f32 v[212:213], v[232:233], v[240:241], v[212:213] op_sel_hi:[1,0,1]
	v_pk_fma_f32 v[214:215], v[234:235], v[240:241], v[214:215] op_sel_hi:[1,0,1]
	v_pk_fma_f32 v[212:213], v[236:237], v[242:243], v[212:213] op_sel_hi:[1,0,1]
	v_pk_fma_f32 v[214:215], v[238:239], v[242:243], v[214:215] op_sel_hi:[1,0,1]
	global_store_dwordx4 v4, v[212:215], s[58:59] offset:1024
	v_cvt_pk_f32_fp8_e32 v[224:225], v70
	v_cvt_pk_f32_fp8_sdwa v[226:227], v70 src0_sel:WORD_1
	v_cvt_pk_f32_fp8_e32 v[228:229], v78
	v_cvt_pk_f32_fp8_sdwa v[230:231], v78 src0_sel:WORD_1
	v_lshlrev_b32_e32 v216, 16, v92
	v_and_b32_e32 v217, 0xffff0000, v92
	v_lshlrev_b32_e32 v218, 16, v93
	v_and_b32_e32 v219, 0xffff0000, v93
	v_pk_fma_f32 v[216:217], v[224:225], v[240:241], v[216:217] op_sel_hi:[1,0,1]
	v_pk_fma_f32 v[218:219], v[226:227], v[240:241], v[218:219] op_sel_hi:[1,0,1]
	v_pk_fma_f32 v[216:217], v[228:229], v[242:243], v[216:217] op_sel_hi:[1,0,1]
	v_pk_fma_f32 v[218:219], v[230:231], v[242:243], v[218:219] op_sel_hi:[1,0,1]
	global_store_dwordx4 v4, v[216:219], s[58:59] offset:2048
	v_cvt_pk_f32_fp8_e32 v[232:233], v71
	v_cvt_pk_f32_fp8_sdwa v[234:235], v71 src0_sel:WORD_1
	v_cvt_pk_f32_fp8_e32 v[236:237], v79
	v_cvt_pk_f32_fp8_sdwa v[238:239], v79 src0_sel:WORD_1
	v_lshlrev_b32_e32 v220, 16, v94
	v_and_b32_e32 v221, 0xffff0000, v94
	v_lshlrev_b32_e32 v222, 16, v95
	v_and_b32_e32 v223, 0xffff0000, v95
	v_pk_fma_f32 v[220:221], v[232:233], v[240:241], v[220:221] op_sel_hi:[1,0,1]
	v_pk_fma_f32 v[222:223], v[234:235], v[240:241], v[222:223] op_sel_hi:[1,0,1]
	v_pk_fma_f32 v[220:221], v[236:237], v[242:243], v[220:221] op_sel_hi:[1,0,1]
	v_pk_fma_f32 v[222:223], v[238:239], v[242:243], v[222:223] op_sel_hi:[1,0,1]
	global_store_dwordx4 v4, v[220:223], s[58:59] offset:3072
	s_waitcnt vmcnt(32)
	s_lshl_b32 s50, s22, 11
	s_add_u32 s50, s48, s50
	s_addc_u32 s51, s49, 0
	s_lshl_b32 s52, s30, 11
	s_add_u32 s52, s48, s52
	s_addc_u32 s53, s49, 0
	s_add_u32 s54, s62, 0x3000000
	s_addc_u32 s55, s63, 0
	global_load_dword v64, v2, s[50:51]
	global_load_dword v65, v2, s[50:51] offset:256
	global_load_dword v66, v2, s[50:51] offset:512
	global_load_dword v67, v2, s[50:51] offset:768
	global_load_dword v68, v2, s[50:51] offset:1024
	global_load_dword v69, v2, s[50:51] offset:1280
	global_load_dword v70, v2, s[50:51] offset:1536
	global_load_dword v71, v2, s[50:51] offset:1792
	global_load_dword v72, v2, s[52:53]
	global_load_dword v73, v2, s[52:53] offset:256
	global_load_dword v74, v2, s[52:53] offset:512
	global_load_dword v75, v2, s[52:53] offset:768
	global_load_dword v76, v2, s[52:53] offset:1024
	global_load_dword v77, v2, s[52:53] offset:1280
	global_load_dword v78, v2, s[52:53] offset:1536
	global_load_dword v79, v2, s[52:53] offset:1792
	global_load_dwordx2 v[80:81], v3, s[54:55]
	global_load_dwordx2 v[82:83], v3, s[54:55] offset:512
	global_load_dwordx2 v[84:85], v3, s[54:55] offset:1024
	global_load_dwordx2 v[86:87], v3, s[54:55] offset:1536
	global_load_dwordx2 v[88:89], v3, s[54:55] offset:2048
	global_load_dwordx2 v[90:91], v3, s[54:55] offset:2560
	global_load_dwordx2 v[92:93], v3, s[54:55] offset:3072
	global_load_dwordx2 v[94:95], v3, s[54:55] offset:3584
	s_add_u32 s56, s64, 0x4000000
	s_addc_u32 s57, s65, 0
	s_add_u32 s58, s56, 0x1000
	s_addc_u32 s59, s57, 0
	v_mov_b32_e32 v240, s36
	v_mov_b32_e32 v242, s44
	v_cvt_pk_f32_fp8_e32 v[224:225], v96
	v_cvt_pk_f32_fp8_sdwa v[226:227], v96 src0_sel:WORD_1
	v_cvt_pk_f32_fp8_e32 v[228:229], v104
	v_cvt_pk_f32_fp8_sdwa v[230:231], v104 src0_sel:WORD_1
	v_lshlrev_b32_e32 v192, 16, v112
	v_and_b32_e32 v193, 0xffff0000, v112
	v_lshlrev_b32_e32 v194, 16, v113
	v_and_b32_e32 v195, 0xffff0000, v113
	v_pk_fma_f32 v[192:193], v[224:225], v[240:241], v[192:193] op_sel_hi:[1,0,1]
	v_pk_fma_f32 v[194:195], v[226:227], v[240:241], v[194:195] op_sel_hi:[1,0,1]
	v_pk_fma_f32 v[192:193], v[228:229], v[242:243], v[192:193] op_sel_hi:[1,0,1]
	v_pk_fma_f32 v[194:195], v[230:231], v[242:243], v[194:195] op_sel_hi:[1,0,1]
	s_waitcnt vmcnt(55)
	global_store_dwordx4 v4, v[192:195], s[56:57]
	v_cvt_pk_f32_fp8_e32 v[232:233], v97
	v_cvt_pk_f32_fp8_sdwa v[234:235], v97 src0_sel:WORD_1
	v_cvt_pk_f32_fp8_e32 v[236:237], v105
	v_cvt_pk_f32_fp8_sdwa v[238:239], v105 src0_sel:WORD_1
	v_lshlrev_b32_e32 v196, 16, v114
	v_and_b32_e32 v197, 0xffff0000, v114
	v_lshlrev_b32_e32 v198, 16, v115
	v_and_b32_e32 v199, 0xffff0000, v115
	v_pk_fma_f32 v[196:197], v[232:233], v[240:241], v[196:197] op_sel_hi:[1,0,1]
	v_pk_fma_f32 v[198:199], v[234:235], v[240:241], v[198:199] op_sel_hi:[1,0,1]
	v_pk_fma_f32 v[196:197], v[236:237], v[242:243], v[196:197] op_sel_hi:[1,0,1]
	v_pk_fma_f32 v[198:199], v[238:239], v[242:243], v[198:199] op_sel_hi:[1,0,1]
	global_store_dwordx4 v4, v[196:199], s[56:57] offset:1024
	v_cvt_pk_f32_fp8_e32 v[224:225], v98
	v_cvt_pk_f32_fp8_sdwa v[226:227], v98 src0_sel:WORD_1
	v_cvt_pk_f32_fp8_e32 v[228:229], v106
	v_cvt_pk_f32_fp8_sdwa v[230:231], v106 src0_sel:WORD_1
	v_lshlrev_b32_e32 v200, 16, v116
	v_and_b32_e32 v201, 0xffff0000, v116
	v_lshlrev_b32_e32 v202, 16, v117
	v_and_b32_e32 v203, 0xffff0000, v117
	v_pk_fma_f32 v[200:201], v[224:225], v[240:241], v[200:201] op_sel_hi:[1,0,1]
	v_pk_fma_f32 v[202:203], v[226:227], v[240:241], v[202:203] op_sel_hi:[1,0,1]
	v_pk_fma_f32 v[200:201], v[228:229], v[242:243], v[200:201] op_sel_hi:[1,0,1]
	v_pk_fma_f32 v[202:203], v[230:231], v[242:243], v[202:203] op_sel_hi:[1,0,1]
	global_store_dwordx4 v4, v[200:203], s[56:57] offset:2048
	v_cvt_pk_f32_fp8_e32 v[232:233], v99
	v_cvt_pk_f32_fp8_sdwa v[234:235], v99 src0_sel:WORD_1
	v_cvt_pk_f32_fp8_e32 v[236:237], v107
	v_cvt_pk_f32_fp8_sdwa v[238:239], v107 src0_sel:WORD_1
	v_lshlrev_b32_e32 v204, 16, v118
	v_and_b32_e32 v205, 0xffff0000, v118
	v_lshlrev_b32_e32 v206, 16, v119
	v_and_b32_e32 v207, 0xffff0000, v119
	v_pk_fma_f32 v[204:205], v[232:233], v[240:241], v[204:205] op_sel_hi:[1,0,1]
	v_pk_fma_f32 v[206:207], v[234:235], v[240:241], v[206:207] op_sel_hi:[1,0,1]
	v_pk_fma_f32 v[204:205], v[236:237], v[242:243], v[204:205] op_sel_hi:[1,0,1]
	v_pk_fma_f32 v[206:207], v[238:239], v[242:243], v[206:207] op_sel_hi:[1,0,1]
	global_store_dwordx4 v4, v[204:207], s[56:57] offset:3072
	v_cvt_pk_f32_fp8_e32 v[224:225], v100
	v_cvt_pk_f32_fp8_sdwa v[226:227], v100 src0_sel:WORD_1
	v_cvt_pk_f32_fp8_e32 v[228:229], v108
	v_cvt_pk_f32_fp8_sdwa v[230:231], v108 src0_sel:WORD_1
	v_lshlrev_b32_e32 v208, 16, v120
	v_and_b32_e32 v209, 0xffff0000, v120
	v_lshlrev_b32_e32 v210, 16, v121
	v_and_b32_e32 v211, 0xffff0000, v121
	v_pk_fma_f32 v[208:209], v[224:225], v[240:241], v[208:209] op_sel_hi:[1,0,1]
	v_pk_fma_f32 v[210:211], v[226:227], v[240:241], v[210:211] op_sel_hi:[1,0,1]
	v_pk_fma_f32 v[208:209], v[228:229], v[242:243], v[208:209] op_sel_hi:[1,0,1]
	v_pk_fma_f32 v[210:211], v[230:231], v[242:243], v[210:211] op_sel_hi:[1,0,1]
	global_store_dwordx4 v4, v[208:211], s[58:59]
	v_cvt_pk_f32_fp8_e32 v[232:233], v101
	v_cvt_pk_f32_fp8_sdwa v[234:235], v101 src0_sel:WORD_1
	v_cvt_pk_f32_fp8_e32 v[236:237], v109
	v_cvt_pk_f32_fp8_sdwa v[238:239], v109 src0_sel:WORD_1
	v_lshlrev_b32_e32 v212, 16, v122
	v_and_b32_e32 v213, 0xffff0000, v122
	v_lshlrev_b32_e32 v214, 16, v123
	v_and_b32_e32 v215, 0xffff0000, v123
	v_pk_fma_f32 v[212:213], v[232:233], v[240:241], v[212:213] op_sel_hi:[1,0,1]
	v_pk_fma_f32 v[214:215], v[234:235], v[240:241], v[214:215] op_sel_hi:[1,0,1]
	v_pk_fma_f32 v[212:213], v[236:237], v[242:243], v[212:213] op_sel_hi:[1,0,1]
	v_pk_fma_f32 v[214:215], v[238:239], v[242:243], v[214:215] op_sel_hi:[1,0,1]
	global_store_dwordx4 v4, v[212:215], s[58:59] offset:1024
	v_cvt_pk_f32_fp8_e32 v[224:225], v102
	v_cvt_pk_f32_fp8_sdwa v[226:227], v102 src0_sel:WORD_1
	v_cvt_pk_f32_fp8_e32 v[228:229], v110
	v_cvt_pk_f32_fp8_sdwa v[230:231], v110 src0_sel:WORD_1
	v_lshlrev_b32_e32 v216, 16, v124
	v_and_b32_e32 v217, 0xffff0000, v124
	v_lshlrev_b32_e32 v218, 16, v125
	v_and_b32_e32 v219, 0xffff0000, v125
	v_pk_fma_f32 v[216:217], v[224:225], v[240:241], v[216:217] op_sel_hi:[1,0,1]
	v_pk_fma_f32 v[218:219], v[226:227], v[240:241], v[218:219] op_sel_hi:[1,0,1]
	v_pk_fma_f32 v[216:217], v[228:229], v[242:243], v[216:217] op_sel_hi:[1,0,1]
	v_pk_fma_f32 v[218:219], v[230:231], v[242:243], v[218:219] op_sel_hi:[1,0,1]
	global_store_dwordx4 v4, v[216:219], s[58:59] offset:2048
	v_cvt_pk_f32_fp8_e32 v[232:233], v103
	v_cvt_pk_f32_fp8_sdwa v[234:235], v103 src0_sel:WORD_1
	v_cvt_pk_f32_fp8_e32 v[236:237], v111
	v_cvt_pk_f32_fp8_sdwa v[238:239], v111 src0_sel:WORD_1
	v_lshlrev_b32_e32 v220, 16, v126
	v_and_b32_e32 v221, 0xffff0000, v126
	v_lshlrev_b32_e32 v222, 16, v127
	v_and_b32_e32 v223, 0xffff0000, v127
	v_pk_fma_f32 v[220:221], v[232:233], v[240:241], v[220:221] op_sel_hi:[1,0,1]
	v_pk_fma_f32 v[222:223], v[234:235], v[240:241], v[222:223] op_sel_hi:[1,0,1]
	v_pk_fma_f32 v[220:221], v[236:237], v[242:243], v[220:221] op_sel_hi:[1,0,1]
	v_pk_fma_f32 v[222:223], v[238:239], v[242:243], v[222:223] op_sel_hi:[1,0,1]
	global_store_dwordx4 v4, v[220:223], s[58:59] offset:3072
	s_waitcnt vmcnt(32)
	s_lshl_b32 s50, s23, 11
	s_add_u32 s50, s48, s50
	s_addc_u32 s51, s49, 0
	s_lshl_b32 s52, s31, 11
	s_add_u32 s52, s48, s52
	s_addc_u32 s53, s49, 0
	s_add_u32 s54, s62, 0x3800000
	s_addc_u32 s55, s63, 0
	global_load_dword v96, v2, s[50:51]
	global_load_dword v97, v2, s[50:51] offset:256
	global_load_dword v98, v2, s[50:51] offset:512
	global_load_dword v99, v2, s[50:51] offset:768
	global_load_dword v100, v2, s[50:51] offset:1024
	global_load_dword v101, v2, s[50:51] offset:1280
	global_load_dword v102, v2, s[50:51] offset:1536
	global_load_dword v103, v2, s[50:51] offset:1792
	global_load_dword v104, v2, s[52:53]
	global_load_dword v105, v2, s[52:53] offset:256
	global_load_dword v106, v2, s[52:53] offset:512
	global_load_dword v107, v2, s[52:53] offset:768
	global_load_dword v108, v2, s[52:53] offset:1024
	global_load_dword v109, v2, s[52:53] offset:1280
	global_load_dword v110, v2, s[52:53] offset:1536
	global_load_dword v111, v2, s[52:53] offset:1792
	global_load_dwordx2 v[112:113], v3, s[54:55]
	global_load_dwordx2 v[114:115], v3, s[54:55] offset:512
	global_load_dwordx2 v[116:117], v3, s[54:55] offset:1024
	global_load_dwordx2 v[118:119], v3, s[54:55] offset:1536
	global_load_dwordx2 v[120:121], v3, s[54:55] offset:2048
	global_load_dwordx2 v[122:123], v3, s[54:55] offset:2560
	global_load_dwordx2 v[124:125], v3, s[54:55] offset:3072
	global_load_dwordx2 v[126:127], v3, s[54:55] offset:3584
	s_add_u32 s56, s64, 0x5000000
	s_addc_u32 s57, s65, 0
	s_add_u32 s58, s56, 0x1000
	s_addc_u32 s59, s57, 0
	v_mov_b32_e32 v240, s37
	v_mov_b32_e32 v242, s45
	v_cvt_pk_f32_fp8_e32 v[224:225], v128
	v_cvt_pk_f32_fp8_sdwa v[226:227], v128 src0_sel:WORD_1
	v_cvt_pk_f32_fp8_e32 v[228:229], v136
	v_cvt_pk_f32_fp8_sdwa v[230:231], v136 src0_sel:WORD_1
	v_lshlrev_b32_e32 v192, 16, v144
	v_and_b32_e32 v193, 0xffff0000, v144
	v_lshlrev_b32_e32 v194, 16, v145
	v_and_b32_e32 v195, 0xffff0000, v145
	v_pk_fma_f32 v[192:193], v[224:225], v[240:241], v[192:193] op_sel_hi:[1,0,1]
	v_pk_fma_f32 v[194:195], v[226:227], v[240:241], v[194:195] op_sel_hi:[1,0,1]
	v_pk_fma_f32 v[192:193], v[228:229], v[242:243], v[192:193] op_sel_hi:[1,0,1]
	v_pk_fma_f32 v[194:195], v[230:231], v[242:243], v[194:195] op_sel_hi:[1,0,1]
	s_waitcnt vmcnt(55)
	global_store_dwordx4 v4, v[192:195], s[56:57]
	v_cvt_pk_f32_fp8_e32 v[232:233], v129
	v_cvt_pk_f32_fp8_sdwa v[234:235], v129 src0_sel:WORD_1
	v_cvt_pk_f32_fp8_e32 v[236:237], v137
	v_cvt_pk_f32_fp8_sdwa v[238:239], v137 src0_sel:WORD_1
	v_lshlrev_b32_e32 v196, 16, v146
	v_and_b32_e32 v197, 0xffff0000, v146
	v_lshlrev_b32_e32 v198, 16, v147
	v_and_b32_e32 v199, 0xffff0000, v147
	v_pk_fma_f32 v[196:197], v[232:233], v[240:241], v[196:197] op_sel_hi:[1,0,1]
	v_pk_fma_f32 v[198:199], v[234:235], v[240:241], v[198:199] op_sel_hi:[1,0,1]
	v_pk_fma_f32 v[196:197], v[236:237], v[242:243], v[196:197] op_sel_hi:[1,0,1]
	v_pk_fma_f32 v[198:199], v[238:239], v[242:243], v[198:199] op_sel_hi:[1,0,1]
	global_store_dwordx4 v4, v[196:199], s[56:57] offset:1024
	v_cvt_pk_f32_fp8_e32 v[224:225], v130
	v_cvt_pk_f32_fp8_sdwa v[226:227], v130 src0_sel:WORD_1
	v_cvt_pk_f32_fp8_e32 v[228:229], v138
	v_cvt_pk_f32_fp8_sdwa v[230:231], v138 src0_sel:WORD_1
	v_lshlrev_b32_e32 v200, 16, v148
	v_and_b32_e32 v201, 0xffff0000, v148
	v_lshlrev_b32_e32 v202, 16, v149
	v_and_b32_e32 v203, 0xffff0000, v149
	v_pk_fma_f32 v[200:201], v[224:225], v[240:241], v[200:201] op_sel_hi:[1,0,1]
	v_pk_fma_f32 v[202:203], v[226:227], v[240:241], v[202:203] op_sel_hi:[1,0,1]
	v_pk_fma_f32 v[200:201], v[228:229], v[242:243], v[200:201] op_sel_hi:[1,0,1]
	v_pk_fma_f32 v[202:203], v[230:231], v[242:243], v[202:203] op_sel_hi:[1,0,1]
	global_store_dwordx4 v4, v[200:203], s[56:57] offset:2048
	v_cvt_pk_f32_fp8_e32 v[232:233], v131
	v_cvt_pk_f32_fp8_sdwa v[234:235], v131 src0_sel:WORD_1
	v_cvt_pk_f32_fp8_e32 v[236:237], v139
	v_cvt_pk_f32_fp8_sdwa v[238:239], v139 src0_sel:WORD_1
	v_lshlrev_b32_e32 v204, 16, v150
	v_and_b32_e32 v205, 0xffff0000, v150
	v_lshlrev_b32_e32 v206, 16, v151
	v_and_b32_e32 v207, 0xffff0000, v151
	v_pk_fma_f32 v[204:205], v[232:233], v[240:241], v[204:205] op_sel_hi:[1,0,1]
	v_pk_fma_f32 v[206:207], v[234:235], v[240:241], v[206:207] op_sel_hi:[1,0,1]
	v_pk_fma_f32 v[204:205], v[236:237], v[242:243], v[204:205] op_sel_hi:[1,0,1]
	v_pk_fma_f32 v[206:207], v[238:239], v[242:243], v[206:207] op_sel_hi:[1,0,1]
	global_store_dwordx4 v4, v[204:207], s[56:57] offset:3072
	v_cvt_pk_f32_fp8_e32 v[224:225], v132
	v_cvt_pk_f32_fp8_sdwa v[226:227], v132 src0_sel:WORD_1
	v_cvt_pk_f32_fp8_e32 v[228:229], v140
	v_cvt_pk_f32_fp8_sdwa v[230:231], v140 src0_sel:WORD_1
	v_lshlrev_b32_e32 v208, 16, v152
	v_and_b32_e32 v209, 0xffff0000, v152
	v_lshlrev_b32_e32 v210, 16, v153
	v_and_b32_e32 v211, 0xffff0000, v153
	v_pk_fma_f32 v[208:209], v[224:225], v[240:241], v[208:209] op_sel_hi:[1,0,1]
	v_pk_fma_f32 v[210:211], v[226:227], v[240:241], v[210:211] op_sel_hi:[1,0,1]
	v_pk_fma_f32 v[208:209], v[228:229], v[242:243], v[208:209] op_sel_hi:[1,0,1]
	v_pk_fma_f32 v[210:211], v[230:231], v[242:243], v[210:211] op_sel_hi:[1,0,1]
	global_store_dwordx4 v4, v[208:211], s[58:59]
	v_cvt_pk_f32_fp8_e32 v[232:233], v133
	v_cvt_pk_f32_fp8_sdwa v[234:235], v133 src0_sel:WORD_1
	v_cvt_pk_f32_fp8_e32 v[236:237], v141
	v_cvt_pk_f32_fp8_sdwa v[238:239], v141 src0_sel:WORD_1
	v_lshlrev_b32_e32 v212, 16, v154
	v_and_b32_e32 v213, 0xffff0000, v154
	v_lshlrev_b32_e32 v214, 16, v155
	v_and_b32_e32 v215, 0xffff0000, v155
	v_pk_fma_f32 v[212:213], v[232:233], v[240:241], v[212:213] op_sel_hi:[1,0,1]
	v_pk_fma_f32 v[214:215], v[234:235], v[240:241], v[214:215] op_sel_hi:[1,0,1]
	v_pk_fma_f32 v[212:213], v[236:237], v[242:243], v[212:213] op_sel_hi:[1,0,1]
	v_pk_fma_f32 v[214:215], v[238:239], v[242:243], v[214:215] op_sel_hi:[1,0,1]
	global_store_dwordx4 v4, v[212:215], s[58:59] offset:1024
	v_cvt_pk_f32_fp8_e32 v[224:225], v134
	v_cvt_pk_f32_fp8_sdwa v[226:227], v134 src0_sel:WORD_1
	v_cvt_pk_f32_fp8_e32 v[228:229], v142
	v_cvt_pk_f32_fp8_sdwa v[230:231], v142 src0_sel:WORD_1
	v_lshlrev_b32_e32 v216, 16, v156
	v_and_b32_e32 v217, 0xffff0000, v156
	v_lshlrev_b32_e32 v218, 16, v157
	v_and_b32_e32 v219, 0xffff0000, v157
	v_pk_fma_f32 v[216:217], v[224:225], v[240:241], v[216:217] op_sel_hi:[1,0,1]
	v_pk_fma_f32 v[218:219], v[226:227], v[240:241], v[218:219] op_sel_hi:[1,0,1]
	v_pk_fma_f32 v[216:217], v[228:229], v[242:243], v[216:217] op_sel_hi:[1,0,1]
	v_pk_fma_f32 v[218:219], v[230:231], v[242:243], v[218:219] op_sel_hi:[1,0,1]
	global_store_dwordx4 v4, v[216:219], s[58:59] offset:2048
	v_cvt_pk_f32_fp8_e32 v[232:233], v135
	v_cvt_pk_f32_fp8_sdwa v[234:235], v135 src0_sel:WORD_1
	v_cvt_pk_f32_fp8_e32 v[236:237], v143
	v_cvt_pk_f32_fp8_sdwa v[238:239], v143 src0_sel:WORD_1
	v_lshlrev_b32_e32 v220, 16, v158
	v_and_b32_e32 v221, 0xffff0000, v158
	v_lshlrev_b32_e32 v222, 16, v159
	v_and_b32_e32 v223, 0xffff0000, v159
	v_pk_fma_f32 v[220:221], v[232:233], v[240:241], v[220:221] op_sel_hi:[1,0,1]
	v_pk_fma_f32 v[222:223], v[234:235], v[240:241], v[222:223] op_sel_hi:[1,0,1]
	v_pk_fma_f32 v[220:221], v[236:237], v[242:243], v[220:221] op_sel_hi:[1,0,1]
	v_pk_fma_f32 v[222:223], v[238:239], v[242:243], v[222:223] op_sel_hi:[1,0,1]
	global_store_dwordx4 v4, v[220:223], s[58:59] offset:3072
	s_waitcnt vmcnt(32)
	s_add_u32 s56, s64, 0x6000000
	s_addc_u32 s57, s65, 0
	s_add_u32 s58, s56, 0x1000
	s_addc_u32 s59, s57, 0
	v_mov_b32_e32 v240, s38
	v_mov_b32_e32 v242, s46
	v_cvt_pk_f32_fp8_e32 v[224:225], v64
	v_cvt_pk_f32_fp8_sdwa v[226:227], v64 src0_sel:WORD_1
	v_cvt_pk_f32_fp8_e32 v[228:229], v72
	v_cvt_pk_f32_fp8_sdwa v[230:231], v72 src0_sel:WORD_1
	v_lshlrev_b32_e32 v192, 16, v80
	v_and_b32_e32 v193, 0xffff0000, v80
	v_lshlrev_b32_e32 v194, 16, v81
	v_and_b32_e32 v195, 0xffff0000, v81
	v_pk_fma_f32 v[192:193], v[224:225], v[240:241], v[192:193] op_sel_hi:[1,0,1]
	v_pk_fma_f32 v[194:195], v[226:227], v[240:241], v[194:195] op_sel_hi:[1,0,1]
	v_pk_fma_f32 v[192:193], v[228:229], v[242:243], v[192:193] op_sel_hi:[1,0,1]
	v_pk_fma_f32 v[194:195], v[230:231], v[242:243], v[194:195] op_sel_hi:[1,0,1]
	s_waitcnt vmcnt(55)
	global_store_dwordx4 v4, v[192:195], s[56:57]
	v_cvt_pk_f32_fp8_e32 v[232:233], v65
	v_cvt_pk_f32_fp8_sdwa v[234:235], v65 src0_sel:WORD_1
	v_cvt_pk_f32_fp8_e32 v[236:237], v73
	v_cvt_pk_f32_fp8_sdwa v[238:239], v73 src0_sel:WORD_1
	v_lshlrev_b32_e32 v196, 16, v82
	v_and_b32_e32 v197, 0xffff0000, v82
	v_lshlrev_b32_e32 v198, 16, v83
	v_and_b32_e32 v199, 0xffff0000, v83
	v_pk_fma_f32 v[196:197], v[232:233], v[240:241], v[196:197] op_sel_hi:[1,0,1]
	v_pk_fma_f32 v[198:199], v[234:235], v[240:241], v[198:199] op_sel_hi:[1,0,1]
	v_pk_fma_f32 v[196:197], v[236:237], v[242:243], v[196:197] op_sel_hi:[1,0,1]
	v_pk_fma_f32 v[198:199], v[238:239], v[242:243], v[198:199] op_sel_hi:[1,0,1]
	global_store_dwordx4 v4, v[196:199], s[56:57] offset:1024
	v_cvt_pk_f32_fp8_e32 v[224:225], v66
	v_cvt_pk_f32_fp8_sdwa v[226:227], v66 src0_sel:WORD_1
	v_cvt_pk_f32_fp8_e32 v[228:229], v74
	v_cvt_pk_f32_fp8_sdwa v[230:231], v74 src0_sel:WORD_1
	v_lshlrev_b32_e32 v200, 16, v84
	v_and_b32_e32 v201, 0xffff0000, v84
	v_lshlrev_b32_e32 v202, 16, v85
	v_and_b32_e32 v203, 0xffff0000, v85
	v_pk_fma_f32 v[200:201], v[224:225], v[240:241], v[200:201] op_sel_hi:[1,0,1]
	v_pk_fma_f32 v[202:203], v[226:227], v[240:241], v[202:203] op_sel_hi:[1,0,1]
	v_pk_fma_f32 v[200:201], v[228:229], v[242:243], v[200:201] op_sel_hi:[1,0,1]
	v_pk_fma_f32 v[202:203], v[230:231], v[242:243], v[202:203] op_sel_hi:[1,0,1]
	global_store_dwordx4 v4, v[200:203], s[56:57] offset:2048
	v_cvt_pk_f32_fp8_e32 v[232:233], v67
	v_cvt_pk_f32_fp8_sdwa v[234:235], v67 src0_sel:WORD_1
	v_cvt_pk_f32_fp8_e32 v[236:237], v75
	v_cvt_pk_f32_fp8_sdwa v[238:239], v75 src0_sel:WORD_1
	v_lshlrev_b32_e32 v204, 16, v86
	v_and_b32_e32 v205, 0xffff0000, v86
	v_lshlrev_b32_e32 v206, 16, v87
	v_and_b32_e32 v207, 0xffff0000, v87
	v_pk_fma_f32 v[204:205], v[232:233], v[240:241], v[204:205] op_sel_hi:[1,0,1]
	v_pk_fma_f32 v[206:207], v[234:235], v[240:241], v[206:207] op_sel_hi:[1,0,1]
	v_pk_fma_f32 v[204:205], v[236:237], v[242:243], v[204:205] op_sel_hi:[1,0,1]
	v_pk_fma_f32 v[206:207], v[238:239], v[242:243], v[206:207] op_sel_hi:[1,0,1]
	global_store_dwordx4 v4, v[204:207], s[56:57] offset:3072
	v_cvt_pk_f32_fp8_e32 v[224:225], v68
	v_cvt_pk_f32_fp8_sdwa v[226:227], v68 src0_sel:WORD_1
	v_cvt_pk_f32_fp8_e32 v[228:229], v76
	v_cvt_pk_f32_fp8_sdwa v[230:231], v76 src0_sel:WORD_1
	v_lshlrev_b32_e32 v208, 16, v88
	v_and_b32_e32 v209, 0xffff0000, v88
	v_lshlrev_b32_e32 v210, 16, v89
	v_and_b32_e32 v211, 0xffff0000, v89
	v_pk_fma_f32 v[208:209], v[224:225], v[240:241], v[208:209] op_sel_hi:[1,0,1]
	v_pk_fma_f32 v[210:211], v[226:227], v[240:241], v[210:211] op_sel_hi:[1,0,1]
	v_pk_fma_f32 v[208:209], v[228:229], v[242:243], v[208:209] op_sel_hi:[1,0,1]
	v_pk_fma_f32 v[210:211], v[230:231], v[242:243], v[210:211] op_sel_hi:[1,0,1]
	global_store_dwordx4 v4, v[208:211], s[58:59]
	v_cvt_pk_f32_fp8_e32 v[232:233], v69
	v_cvt_pk_f32_fp8_sdwa v[234:235], v69 src0_sel:WORD_1
	v_cvt_pk_f32_fp8_e32 v[236:237], v77
	v_cvt_pk_f32_fp8_sdwa v[238:239], v77 src0_sel:WORD_1
	v_lshlrev_b32_e32 v212, 16, v90
	v_and_b32_e32 v213, 0xffff0000, v90
	v_lshlrev_b32_e32 v214, 16, v91
	v_and_b32_e32 v215, 0xffff0000, v91
	v_pk_fma_f32 v[212:213], v[232:233], v[240:241], v[212:213] op_sel_hi:[1,0,1]
	v_pk_fma_f32 v[214:215], v[234:235], v[240:241], v[214:215] op_sel_hi:[1,0,1]
	v_pk_fma_f32 v[212:213], v[236:237], v[242:243], v[212:213] op_sel_hi:[1,0,1]
	v_pk_fma_f32 v[214:215], v[238:239], v[242:243], v[214:215] op_sel_hi:[1,0,1]
	global_store_dwordx4 v4, v[212:215], s[58:59] offset:1024
	v_cvt_pk_f32_fp8_e32 v[224:225], v70
	v_cvt_pk_f32_fp8_sdwa v[226:227], v70 src0_sel:WORD_1
	v_cvt_pk_f32_fp8_e32 v[228:229], v78
	v_cvt_pk_f32_fp8_sdwa v[230:231], v78 src0_sel:WORD_1
	v_lshlrev_b32_e32 v216, 16, v92
	v_and_b32_e32 v217, 0xffff0000, v92
	v_lshlrev_b32_e32 v218, 16, v93
	v_and_b32_e32 v219, 0xffff0000, v93
	v_pk_fma_f32 v[216:217], v[224:225], v[240:241], v[216:217] op_sel_hi:[1,0,1]
	v_pk_fma_f32 v[218:219], v[226:227], v[240:241], v[218:219] op_sel_hi:[1,0,1]
	v_pk_fma_f32 v[216:217], v[228:229], v[242:243], v[216:217] op_sel_hi:[1,0,1]
	v_pk_fma_f32 v[218:219], v[230:231], v[242:243], v[218:219] op_sel_hi:[1,0,1]
	global_store_dwordx4 v4, v[216:219], s[58:59] offset:2048
	v_cvt_pk_f32_fp8_e32 v[232:233], v71
	v_cvt_pk_f32_fp8_sdwa v[234:235], v71 src0_sel:WORD_1
	v_cvt_pk_f32_fp8_e32 v[236:237], v79
	v_cvt_pk_f32_fp8_sdwa v[238:239], v79 src0_sel:WORD_1
	v_lshlrev_b32_e32 v220, 16, v94
	v_and_b32_e32 v221, 0xffff0000, v94
	v_lshlrev_b32_e32 v222, 16, v95
	v_and_b32_e32 v223, 0xffff0000, v95
	v_pk_fma_f32 v[220:221], v[232:233], v[240:241], v[220:221] op_sel_hi:[1,0,1]
	v_pk_fma_f32 v[222:223], v[234:235], v[240:241], v[222:223] op_sel_hi:[1,0,1]
	v_pk_fma_f32 v[220:221], v[236:237], v[242:243], v[220:221] op_sel_hi:[1,0,1]
	v_pk_fma_f32 v[222:223], v[238:239], v[242:243], v[222:223] op_sel_hi:[1,0,1]
	global_store_dwordx4 v4, v[220:223], s[58:59] offset:3072
	s_waitcnt vmcnt(16)
	s_add_u32 s56, s64, 0x7000000
	s_addc_u32 s57, s65, 0
	s_add_u32 s58, s56, 0x1000
	s_addc_u32 s59, s57, 0
	v_mov_b32_e32 v240, s39
	v_mov_b32_e32 v242, s47
	v_cvt_pk_f32_fp8_e32 v[224:225], v96
	v_cvt_pk_f32_fp8_sdwa v[226:227], v96 src0_sel:WORD_1
	v_cvt_pk_f32_fp8_e32 v[228:229], v104
	v_cvt_pk_f32_fp8_sdwa v[230:231], v104 src0_sel:WORD_1
	v_lshlrev_b32_e32 v192, 16, v112
	v_and_b32_e32 v193, 0xffff0000, v112
	v_lshlrev_b32_e32 v194, 16, v113
	v_and_b32_e32 v195, 0xffff0000, v113
	v_pk_fma_f32 v[192:193], v[224:225], v[240:241], v[192:193] op_sel_hi:[1,0,1]
	v_pk_fma_f32 v[194:195], v[226:227], v[240:241], v[194:195] op_sel_hi:[1,0,1]
	v_pk_fma_f32 v[192:193], v[228:229], v[242:243], v[192:193] op_sel_hi:[1,0,1]
	v_pk_fma_f32 v[194:195], v[230:231], v[242:243], v[194:195] op_sel_hi:[1,0,1]
	s_waitcnt vmcnt(55)
	global_store_dwordx4 v4, v[192:195], s[56:57]
	v_cvt_pk_f32_fp8_e32 v[232:233], v97
	v_cvt_pk_f32_fp8_sdwa v[234:235], v97 src0_sel:WORD_1
	v_cvt_pk_f32_fp8_e32 v[236:237], v105
	v_cvt_pk_f32_fp8_sdwa v[238:239], v105 src0_sel:WORD_1
	v_lshlrev_b32_e32 v196, 16, v114
	v_and_b32_e32 v197, 0xffff0000, v114
	v_lshlrev_b32_e32 v198, 16, v115
	v_and_b32_e32 v199, 0xffff0000, v115
	v_pk_fma_f32 v[196:197], v[232:233], v[240:241], v[196:197] op_sel_hi:[1,0,1]
	v_pk_fma_f32 v[198:199], v[234:235], v[240:241], v[198:199] op_sel_hi:[1,0,1]
	v_pk_fma_f32 v[196:197], v[236:237], v[242:243], v[196:197] op_sel_hi:[1,0,1]
	v_pk_fma_f32 v[198:199], v[238:239], v[242:243], v[198:199] op_sel_hi:[1,0,1]
	global_store_dwordx4 v4, v[196:199], s[56:57] offset:1024
	v_cvt_pk_f32_fp8_e32 v[224:225], v98
	v_cvt_pk_f32_fp8_sdwa v[226:227], v98 src0_sel:WORD_1
	v_cvt_pk_f32_fp8_e32 v[228:229], v106
	v_cvt_pk_f32_fp8_sdwa v[230:231], v106 src0_sel:WORD_1
	v_lshlrev_b32_e32 v200, 16, v116
	v_and_b32_e32 v201, 0xffff0000, v116
	v_lshlrev_b32_e32 v202, 16, v117
	v_and_b32_e32 v203, 0xffff0000, v117
	v_pk_fma_f32 v[200:201], v[224:225], v[240:241], v[200:201] op_sel_hi:[1,0,1]
	v_pk_fma_f32 v[202:203], v[226:227], v[240:241], v[202:203] op_sel_hi:[1,0,1]
	v_pk_fma_f32 v[200:201], v[228:229], v[242:243], v[200:201] op_sel_hi:[1,0,1]
	v_pk_fma_f32 v[202:203], v[230:231], v[242:243], v[202:203] op_sel_hi:[1,0,1]
	global_store_dwordx4 v4, v[200:203], s[56:57] offset:2048
	v_cvt_pk_f32_fp8_e32 v[232:233], v99
	v_cvt_pk_f32_fp8_sdwa v[234:235], v99 src0_sel:WORD_1
	v_cvt_pk_f32_fp8_e32 v[236:237], v107
	v_cvt_pk_f32_fp8_sdwa v[238:239], v107 src0_sel:WORD_1
	v_lshlrev_b32_e32 v204, 16, v118
	v_and_b32_e32 v205, 0xffff0000, v118
	v_lshlrev_b32_e32 v206, 16, v119
	v_and_b32_e32 v207, 0xffff0000, v119
	v_pk_fma_f32 v[204:205], v[232:233], v[240:241], v[204:205] op_sel_hi:[1,0,1]
	v_pk_fma_f32 v[206:207], v[234:235], v[240:241], v[206:207] op_sel_hi:[1,0,1]
	v_pk_fma_f32 v[204:205], v[236:237], v[242:243], v[204:205] op_sel_hi:[1,0,1]
	v_pk_fma_f32 v[206:207], v[238:239], v[242:243], v[206:207] op_sel_hi:[1,0,1]
	global_store_dwordx4 v4, v[204:207], s[56:57] offset:3072
	v_cvt_pk_f32_fp8_e32 v[224:225], v100
	v_cvt_pk_f32_fp8_sdwa v[226:227], v100 src0_sel:WORD_1
	v_cvt_pk_f32_fp8_e32 v[228:229], v108
	v_cvt_pk_f32_fp8_sdwa v[230:231], v108 src0_sel:WORD_1
	v_lshlrev_b32_e32 v208, 16, v120
	v_and_b32_e32 v209, 0xffff0000, v120
	v_lshlrev_b32_e32 v210, 16, v121
	v_and_b32_e32 v211, 0xffff0000, v121
	v_pk_fma_f32 v[208:209], v[224:225], v[240:241], v[208:209] op_sel_hi:[1,0,1]
	v_pk_fma_f32 v[210:211], v[226:227], v[240:241], v[210:211] op_sel_hi:[1,0,1]
	v_pk_fma_f32 v[208:209], v[228:229], v[242:243], v[208:209] op_sel_hi:[1,0,1]
	v_pk_fma_f32 v[210:211], v[230:231], v[242:243], v[210:211] op_sel_hi:[1,0,1]
	global_store_dwordx4 v4, v[208:211], s[58:59]
	v_cvt_pk_f32_fp8_e32 v[232:233], v101
	v_cvt_pk_f32_fp8_sdwa v[234:235], v101 src0_sel:WORD_1
	v_cvt_pk_f32_fp8_e32 v[236:237], v109
	v_cvt_pk_f32_fp8_sdwa v[238:239], v109 src0_sel:WORD_1
	v_lshlrev_b32_e32 v212, 16, v122
	v_and_b32_e32 v213, 0xffff0000, v122
	v_lshlrev_b32_e32 v214, 16, v123
	v_and_b32_e32 v215, 0xffff0000, v123
	v_pk_fma_f32 v[212:213], v[232:233], v[240:241], v[212:213] op_sel_hi:[1,0,1]
	v_pk_fma_f32 v[214:215], v[234:235], v[240:241], v[214:215] op_sel_hi:[1,0,1]
	v_pk_fma_f32 v[212:213], v[236:237], v[242:243], v[212:213] op_sel_hi:[1,0,1]
	v_pk_fma_f32 v[214:215], v[238:239], v[242:243], v[214:215] op_sel_hi:[1,0,1]
	global_store_dwordx4 v4, v[212:215], s[58:59] offset:1024
	v_cvt_pk_f32_fp8_e32 v[224:225], v102
	v_cvt_pk_f32_fp8_sdwa v[226:227], v102 src0_sel:WORD_1
	v_cvt_pk_f32_fp8_e32 v[228:229], v110
	v_cvt_pk_f32_fp8_sdwa v[230:231], v110 src0_sel:WORD_1
	v_lshlrev_b32_e32 v216, 16, v124
	v_and_b32_e32 v217, 0xffff0000, v124
	v_lshlrev_b32_e32 v218, 16, v125
	v_and_b32_e32 v219, 0xffff0000, v125
	v_pk_fma_f32 v[216:217], v[224:225], v[240:241], v[216:217] op_sel_hi:[1,0,1]
	v_pk_fma_f32 v[218:219], v[226:227], v[240:241], v[218:219] op_sel_hi:[1,0,1]
	v_pk_fma_f32 v[216:217], v[228:229], v[242:243], v[216:217] op_sel_hi:[1,0,1]
	v_pk_fma_f32 v[218:219], v[230:231], v[242:243], v[218:219] op_sel_hi:[1,0,1]
	global_store_dwordx4 v4, v[216:219], s[58:59] offset:2048
	v_cvt_pk_f32_fp8_e32 v[232:233], v103
	v_cvt_pk_f32_fp8_sdwa v[234:235], v103 src0_sel:WORD_1
	v_cvt_pk_f32_fp8_e32 v[236:237], v111
	v_cvt_pk_f32_fp8_sdwa v[238:239], v111 src0_sel:WORD_1
	v_lshlrev_b32_e32 v220, 16, v126
	v_and_b32_e32 v221, 0xffff0000, v126
	v_lshlrev_b32_e32 v222, 16, v127
	v_and_b32_e32 v223, 0xffff0000, v127
	v_pk_fma_f32 v[220:221], v[232:233], v[240:241], v[220:221] op_sel_hi:[1,0,1]
	v_pk_fma_f32 v[222:223], v[234:235], v[240:241], v[222:223] op_sel_hi:[1,0,1]
	v_pk_fma_f32 v[220:221], v[236:237], v[242:243], v[220:221] op_sel_hi:[1,0,1]
	v_pk_fma_f32 v[222:223], v[238:239], v[242:243], v[222:223] op_sel_hi:[1,0,1]
	global_store_dwordx4 v4, v[220:223], s[58:59] offset:3072
